# MoE2 scatter epilogue: slot loads hoisted; out-proj epilogue: h0b tile prefetched at head; passA/B counted waits
# baseline (speedup 1.0000x reference)
; __device__ __forceinline__ unsigned cvt_pk_bf16(float lo, float hi) { const f32x2 v = {lo, hi}; return __builtin_bit_cast(unsigned, __builtin_convertvector(v, bf16x2_t)); }
; __device__ __forceinline__ float bflo(unsigned w) { return __uint_as_float(w << 16); }
; __device__ __forceinline__ float bfhi(unsigned w) { return __uint_as_float(w & 0xffff0000u); }
;     __device__ __forceinline__ void operator()(Acc& acc, const GUnit& u, int wr, int wc, int fr, int fq, LAS unsigned char*, int, int) const {
;     ...
;             for (int m = 0; m < 4; ++m) { const int row = row0 + ai * HALF + m * 16; float ps = 0.f, pq = 0.f;
; #pragma unroll
;                 for (int bj = 0; bj < 2; ++bj) { const size_t o = (size_t)row * DM + col0 + bj * HALF; const u32x4 hw = *(const u32x4*)(h0b + o);
;                     const f32x4 s0 = (f32x4){bflo(hw.x), bfhi(hw.x), bflo(hw.y), bfhi(hw.y)} * ALPHA + acc[ai][bj][m][0], s1 = (f32x4){bflo(hw.z), bfhi(hw.z), bflo(hw.w), bfhi(hw.w)} * ALPHA + acc[ai][bj][m][1];
;                     ps += ((s0[0] + s0[1]) + (s0[2] + s0[3])) + ((s1[0] + s1[1]) + (s1[2] + s1[3]));
;                     pq += ((s0[0] * s0[0] + s0[1] * s0[1]) + (s0[2] * s0[2] + s0[3] * s0[3])) + ((s1[0] * s1[0] + s1[1] * s1[1]) + (s1[2] * s1[2] + s1[3] * s1[3]));
;                     u32x4 w; w.x = cvt_pk_bf16(s0[0], s0[1]); w.y = cvt_pk_bf16(s0[2], s0[3]); w.z = cvt_pk_bf16(s1[0], s1[1]); w.w = cvt_pk_bf16(s1[2], s1[3]); *(u32x4*)(S + o) = w; }
;                 ps = xrow_sum(ps); pq = xrow_sum(pq);
;                 if (fq == 0) *(f32x2*)(part + ((size_t)row * 32 + u.pn * 4 + wc) * 2) = (f32x2){ps, pq}; }
.LBB0_833:
	v_add_u32_e32 v148, s53, v1
	v_add_u32_e32 v146, s54, v151
	v_ashrrev_i32_e32 v149, 31, v148
	v_ashrrev_i32_e32 v147, 31, v146
	v_lshlrev_b64 v[156:157], 11, v[148:149]
	v_lshl_add_u64 v[156:157], v[156:157], 0, v[146:147]
	v_lshlrev_b64 v[164:165], 1, v[156:157]
	v_lshl_add_u64 v[160:161], s[18:19], 0, v[164:165]
	s_mov_b64 s[98:99], 0x10000
	s_mov_b64 s[100:101], 0x80000
	v_lshl_add_u64 v[252:253], v[160:161], 0, s[98:99]
	global_load_dwordx4 v[184:187], v[252:253], off
	global_load_dwordx4 v[188:191], v[252:253], off offset:256
	v_lshl_add_u64 v[252:253], v[252:253], 0, s[98:99]
	global_load_dwordx4 v[192:195], v[252:253], off
	global_load_dwordx4 v[196:199], v[252:253], off offset:256
	v_lshl_add_u64 v[252:253], v[252:253], 0, s[98:99]
	global_load_dwordx4 v[200:203], v[252:253], off
	global_load_dwordx4 v[204:207], v[252:253], off offset:256
	v_lshl_add_u64 v[252:253], v[160:161], 0, s[100:101]
	global_load_dwordx4 v[208:211], v[252:253], off
	global_load_dwordx4 v[212:215], v[252:253], off offset:256
	v_lshl_add_u64 v[252:253], v[252:253], 0, s[98:99]
	global_load_dwordx4 v[216:219], v[252:253], off
	global_load_dwordx4 v[220:223], v[252:253], off offset:256
	v_lshl_add_u64 v[252:253], v[252:253], 0, s[98:99]
	global_load_dwordx4 v[224:227], v[252:253], off
	global_load_dwordx4 v[228:231], v[252:253], off offset:256
	v_lshl_add_u64 v[252:253], v[252:253], 0, s[98:99]
	global_load_dwordx4 v[232:235], v[252:253], off
	global_load_dwordx4 v[236:239], v[252:253], off offset:256
	global_load_dwordx4 v[156:159], v[160:161], off
	s_nop 0
	global_load_dwordx4 v[160:163], v[160:161], off offset:256
	v_lshl_add_u64 v[164:165], s[16:17], 0, v[164:165]
	s_waitcnt vmcnt(0)
	v_lshlrev_b32_e32 v166, 16, v156
	v_and_b32_e32 v167, 0xffff0000, v156
	v_lshlrev_b32_e32 v156, 16, v157
	v_and_b32_e32 v157, 0xffff0000, v157
	v_lshlrev_b32_e32 v168, 16, v158
	v_and_b32_e32 v169, 0xffff0000, v158
	v_lshlrev_b32_e32 v158, 16, v159
	v_and_b32_e32 v159, 0xffff0000, v159
	v_lshlrev_b32_e32 v170, 16, v160
	v_and_b32_e32 v171, 0xffff0000, v160
	v_lshlrev_b32_e32 v160, 16, v161
	v_and_b32_e32 v161, 0xffff0000, v161
	v_lshlrev_b32_e32 v172, 16, v162
	v_and_b32_e32 v173, 0xffff0000, v162
	v_lshlrev_b32_e32 v162, 16, v163
	v_and_b32_e32 v163, 0xffff0000, v163
	v_pk_fma_f32 v[128:129], v[156:157], s[30:31], v[128:129] op_sel_hi:[1,0,1]
	v_pk_fma_f32 v[126:127], v[166:167], s[30:31], v[126:127] op_sel_hi:[1,0,1]
	v_pk_fma_f32 v[124:125], v[158:159], s[30:31], v[124:125] op_sel_hi:[1,0,1]
	v_pk_fma_f32 v[122:123], v[168:169], s[30:31], v[122:123] op_sel_hi:[1,0,1]
	v_pk_fma_f32 v[156:157], v[160:161], s[30:31], v[120:121] op_sel_hi:[1,0,1]
	v_pk_fma_f32 v[158:159], v[170:171], s[30:31], v[118:119] op_sel_hi:[1,0,1]
	v_pk_fma_f32 v[160:161], v[162:163], s[30:31], v[116:117] op_sel_hi:[1,0,1]
	v_pk_fma_f32 v[162:163], v[172:173], s[30:31], v[114:115] op_sel_hi:[1,0,1]
	v_add_f32_e32 v155, v126, v127
	v_add_f32_e32 v166, v128, v129
	v_add_f32_e32 v167, v122, v123
	v_add_f32_e32 v168, v124, v125
	v_mul_f32_e32 v169, v127, v127
	v_mul_f32_e32 v170, v129, v129
	v_mul_f32_e32 v171, v123, v123
	v_mul_f32_e32 v172, v125, v125
	v_cvt_pk_bf16_f32 v114, v126, v127
	v_cvt_pk_bf16_f32 v115, v128, v129
	v_cvt_pk_bf16_f32 v116, v122, v123
	v_cvt_pk_bf16_f32 v117, v124, v125
	v_add_f32_e32 v123, v158, v159
	v_add_f32_e32 v125, v156, v157
	v_add_f32_e32 v127, v162, v163
	v_add_f32_e32 v129, v160, v161
	v_mul_f32_e32 v173, v159, v159
	v_mul_f32_e32 v174, v157, v157
	v_mul_f32_e32 v175, v163, v163
	v_mul_f32_e32 v176, v161, v161
	v_cvt_pk_bf16_f32 v118, v158, v159
	v_cvt_pk_bf16_f32 v119, v156, v157
	v_cvt_pk_bf16_f32 v120, v162, v163
	v_cvt_pk_bf16_f32 v121, v160, v161
	v_add_f32_e32 v155, v155, v166
	v_add_f32_e32 v157, v167, v168
	v_fmac_f32_e32 v169, v126, v126
	v_fmac_f32_e32 v170, v128, v128
	v_fmac_f32_e32 v171, v122, v122
	v_fmac_f32_e32 v172, v124, v124
	global_store_dwordx4 v[164:165], v[114:117], off
	v_fmac_f32_e32 v173, v158, v158
	v_fmac_f32_e32 v174, v156, v156
	v_add_f32_e32 v114, v123, v125
	v_add_f32_e32 v115, v127, v129
	v_fmac_f32_e32 v175, v162, v162
	v_fmac_f32_e32 v176, v160, v160
	global_store_dwordx4 v[164:165], v[118:121], off offset:256
	v_add_f32_e32 v116, v155, v157
	v_add_f32_e32 v117, v169, v170
	v_add_f32_e32 v118, v171, v172
	v_add_f32_e32 v114, v114, v115
	v_add_f32_e32 v115, v173, v174
	v_add_f32_e32 v119, v175, v176
	v_add_f32_e32 v116, 0, v116
	v_add_f32_e32 v117, v117, v118
	v_add_f32_e32 v115, v115, v119
	v_add_f32_e32 v114, v116, v114
	v_add_f32_e32 v115, v117, v115
	v_mov_b32_e32 v116, v114
	v_mov_b32_e32 v117, v115
	s_nop 0
	v_permlane16_swap_b32_e32 v114, v116
	v_permlane16_swap_b32_e32 v115, v117
	v_add_f32_e32 v114, v114, v116
	v_add_f32_e32 v115, v115, v117
	v_mov_b32_e32 v116, v114
	v_mov_b32_e32 v117, v115
	s_nop 0
	v_permlane32_swap_b32_e32 v114, v116
	v_permlane32_swap_b32_e32 v115, v117
	s_and_saveexec_b64 s[40:41], s[10:11]
	s_cbranch_execz .LBB0_835
	s_lshl_b32 s42, s4, 2
	v_pk_add_f32 v[114:115], v[114:115], v[116:117]
	v_lshlrev_b64 v[116:117], 5, v[148:149]
	s_ashr_i32 s43, s42, 31
	v_lshl_add_u64 v[116:117], v[116:117], 0, s[42:43]
	v_or_b32_e32 v116, s33, v116
	v_lshl_add_u64 v[116:117], v[116:117], 3, s[20:21]
	global_store_dwordx2 v[116:117], v[114:115], off
; __device__ __forceinline__ unsigned cvt_pk_bf16(float lo, float hi) { const f32x2 v = {lo, hi}; return __builtin_bit_cast(unsigned, __builtin_convertvector(v, bf16x2_t)); }
; __device__ __forceinline__ float bflo(unsigned w) { return __uint_as_float(w << 16); }
; __device__ __forceinline__ float bfhi(unsigned w) { return __uint_as_float(w & 0xffff0000u); }
;     __device__ __forceinline__ void operator()(Acc& acc, const GUnit& u, int wr, int wc, int fr, int fq, LAS unsigned char*, int, int) const {
;     ...
;             for (int m = 0; m < 4; ++m) { const int row = row0 + ai * HALF + m * 16; float ps = 0.f, pq = 0.f;
; #pragma unroll
;                 for (int bj = 0; bj < 2; ++bj) { const size_t o = (size_t)row * DM + col0 + bj * HALF; const u32x4 hw = *(const u32x4*)(h0b + o);
;                     const f32x4 s0 = (f32x4){bflo(hw.x), bfhi(hw.x), bflo(hw.y), bfhi(hw.y)} * ALPHA + acc[ai][bj][m][0], s1 = (f32x4){bflo(hw.z), bfhi(hw.z), bflo(hw.w), bfhi(hw.w)} * ALPHA + acc[ai][bj][m][1];
;                     ps += ((s0[0] + s0[1]) + (s0[2] + s0[3])) + ((s1[0] + s1[1]) + (s1[2] + s1[3]));
;                     pq += ((s0[0] * s0[0] + s0[1] * s0[1]) + (s0[2] * s0[2] + s0[3] * s0[3])) + ((s1[0] * s1[0] + s1[1] * s1[1]) + (s1[2] * s1[2] + s1[3] * s1[3]));
;                     u32x4 w; w.x = cvt_pk_bf16(s0[0], s0[1]); w.y = cvt_pk_bf16(s0[2], s0[3]); w.z = cvt_pk_bf16(s1[0], s1[1]); w.w = cvt_pk_bf16(s1[2], s1[3]); *(u32x4*)(S + o) = w; }
;                 ps = xrow_sum(ps); pq = xrow_sum(pq);
;                 if (fq == 0) *(f32x2*)(part + ((size_t)row * 32 + u.pn * 4 + wc) * 2) = (f32x2){ps, pq}; }
.LBB0_835:
	s_or_b64 exec, exec, s[40:41]
	v_add_u32_e32 v114, 16, v148
	v_ashrrev_i32_e32 v115, 31, v114
	v_lshlrev_b64 v[116:117], 11, v[114:115]
	v_lshl_add_u64 v[116:117], v[116:117], 0, v[146:147]
	v_lshlrev_b64 v[124:125], 1, v[116:117]
	v_lshl_add_u64 v[120:121], s[18:19], 0, v[124:125]
	v_mov_b32_e32 v116, v184
	v_mov_b32_e32 v117, v185
	v_mov_b32_e32 v118, v186
	v_mov_b32_e32 v119, v187
	s_nop 0
	v_mov_b32_e32 v120, v188
	v_mov_b32_e32 v121, v189
	v_mov_b32_e32 v122, v190
	v_mov_b32_e32 v123, v191
	v_lshl_add_u64 v[124:125], s[16:17], 0, v[124:125]
	v_lshlrev_b32_e32 v126, 16, v116
	v_and_b32_e32 v127, 0xffff0000, v116
	v_lshlrev_b32_e32 v116, 16, v117
	v_and_b32_e32 v117, 0xffff0000, v117
	v_lshlrev_b32_e32 v128, 16, v118
	v_and_b32_e32 v129, 0xffff0000, v118
	v_lshlrev_b32_e32 v118, 16, v119
	v_and_b32_e32 v119, 0xffff0000, v119
	v_lshlrev_b32_e32 v156, 16, v120
	v_and_b32_e32 v157, 0xffff0000, v120
	v_lshlrev_b32_e32 v120, 16, v121
	v_and_b32_e32 v121, 0xffff0000, v121
	v_lshlrev_b32_e32 v158, 16, v122
	v_and_b32_e32 v159, 0xffff0000, v122
	v_lshlrev_b32_e32 v122, 16, v123
	v_and_b32_e32 v123, 0xffff0000, v123
	v_pk_fma_f32 v[112:113], v[116:117], s[30:31], v[112:113] op_sel_hi:[1,0,1]
	v_pk_fma_f32 v[110:111], v[126:127], s[30:31], v[110:111] op_sel_hi:[1,0,1]
	v_pk_fma_f32 v[108:109], v[118:119], s[30:31], v[108:109] op_sel_hi:[1,0,1]
	v_pk_fma_f32 v[106:107], v[128:129], s[30:31], v[106:107] op_sel_hi:[1,0,1]
	v_pk_fma_f32 v[116:117], v[120:121], s[30:31], v[104:105] op_sel_hi:[1,0,1]
	v_pk_fma_f32 v[118:119], v[156:157], s[30:31], v[102:103] op_sel_hi:[1,0,1]
	v_pk_fma_f32 v[120:121], v[122:123], s[30:31], v[100:101] op_sel_hi:[1,0,1]
	v_pk_fma_f32 v[122:123], v[158:159], s[30:31], v[98:99] op_sel_hi:[1,0,1]
	v_add_f32_e32 v126, v110, v111
	v_add_f32_e32 v127, v112, v113
	v_add_f32_e32 v128, v106, v107
	v_add_f32_e32 v129, v108, v109
	v_mul_f32_e32 v149, v111, v111
	v_mul_f32_e32 v155, v113, v113
	v_mul_f32_e32 v156, v107, v107
	v_mul_f32_e32 v157, v109, v109
	v_cvt_pk_bf16_f32 v98, v110, v111
	v_cvt_pk_bf16_f32 v99, v112, v113
	v_cvt_pk_bf16_f32 v100, v106, v107
	v_cvt_pk_bf16_f32 v101, v108, v109
	v_add_f32_e32 v107, v118, v119
	v_add_f32_e32 v109, v116, v117
	v_add_f32_e32 v111, v122, v123
	v_add_f32_e32 v113, v120, v121
	v_mul_f32_e32 v158, v119, v119
	v_mul_f32_e32 v159, v117, v117
	v_mul_f32_e32 v160, v123, v123
	v_mul_f32_e32 v161, v121, v121
	v_cvt_pk_bf16_f32 v102, v118, v119
	v_cvt_pk_bf16_f32 v103, v116, v117
	v_cvt_pk_bf16_f32 v104, v122, v123
	v_cvt_pk_bf16_f32 v105, v120, v121
	v_add_f32_e32 v117, v126, v127
	v_add_f32_e32 v119, v128, v129
	v_fmac_f32_e32 v149, v110, v110
	v_fmac_f32_e32 v155, v112, v112
	v_fmac_f32_e32 v156, v106, v106
	v_fmac_f32_e32 v157, v108, v108
	global_store_dwordx4 v[124:125], v[98:101], off
	v_fmac_f32_e32 v158, v118, v118
	v_fmac_f32_e32 v159, v116, v116
	v_add_f32_e32 v98, v107, v109
	v_add_f32_e32 v99, v111, v113
	v_fmac_f32_e32 v160, v122, v122
	v_fmac_f32_e32 v161, v120, v120
	global_store_dwordx4 v[124:125], v[102:105], off offset:256
	v_add_f32_e32 v100, v117, v119
	v_add_f32_e32 v101, v149, v155
	v_add_f32_e32 v102, v156, v157
	v_add_f32_e32 v98, v98, v99
	v_add_f32_e32 v99, v158, v159
	v_add_f32_e32 v103, v160, v161
	v_add_f32_e32 v100, 0, v100
	v_add_f32_e32 v101, v101, v102
	v_add_f32_e32 v99, v99, v103
	v_add_f32_e32 v98, v100, v98
	v_add_f32_e32 v99, v101, v99
	v_mov_b32_e32 v100, v98
	v_mov_b32_e32 v101, v99
	s_nop 0
	v_permlane16_swap_b32_e32 v98, v100
	v_permlane16_swap_b32_e32 v99, v101
	v_add_f32_e32 v98, v98, v100
	v_add_f32_e32 v99, v99, v101
	v_mov_b32_e32 v100, v98
	v_mov_b32_e32 v101, v99
	s_nop 0
	v_permlane32_swap_b32_e32 v98, v100
	v_permlane32_swap_b32_e32 v99, v101
	s_and_saveexec_b64 s[40:41], s[10:11]
	s_cbranch_execz .LBB0_837
	s_lshl_b32 s42, s4, 2
	v_pk_add_f32 v[98:99], v[98:99], v[100:101]
	v_lshlrev_b64 v[100:101], 5, v[114:115]
	s_ashr_i32 s43, s42, 31
	v_lshl_add_u64 v[100:101], v[100:101], 0, s[42:43]
	v_or_b32_e32 v100, s33, v100
	v_lshl_add_u64 v[100:101], v[100:101], 3, s[20:21]
	global_store_dwordx2 v[100:101], v[98:99], off
.LBB0_837:
	s_or_b64 exec, exec, s[40:41]
	v_add_u32_e32 v98, 32, v148
	v_ashrrev_i32_e32 v99, 31, v98
	v_lshlrev_b64 v[100:101], 11, v[98:99]
	v_lshl_add_u64 v[100:101], v[100:101], 0, v[146:147]
	v_lshlrev_b64 v[108:109], 1, v[100:101]
	v_lshl_add_u64 v[104:105], s[18:19], 0, v[108:109]
	v_mov_b32_e32 v100, v192
	v_mov_b32_e32 v101, v193
	v_mov_b32_e32 v102, v194
	v_mov_b32_e32 v103, v195
	s_nop 0
	v_mov_b32_e32 v104, v196
	v_mov_b32_e32 v105, v197
	v_mov_b32_e32 v106, v198
	v_mov_b32_e32 v107, v199
	v_lshl_add_u64 v[108:109], s[16:17], 0, v[108:109]
	v_lshlrev_b32_e32 v110, 16, v100
	v_and_b32_e32 v111, 0xffff0000, v100
	v_lshlrev_b32_e32 v100, 16, v101
	v_and_b32_e32 v101, 0xffff0000, v101
	v_lshlrev_b32_e32 v112, 16, v102
	v_and_b32_e32 v113, 0xffff0000, v102
	v_lshlrev_b32_e32 v102, 16, v103
	v_and_b32_e32 v103, 0xffff0000, v103
	v_lshlrev_b32_e32 v114, 16, v104
	v_and_b32_e32 v115, 0xffff0000, v104
	v_lshlrev_b32_e32 v104, 16, v105
	v_and_b32_e32 v105, 0xffff0000, v105
	v_lshlrev_b32_e32 v116, 16, v106
	v_and_b32_e32 v117, 0xffff0000, v106
	v_lshlrev_b32_e32 v106, 16, v107
	v_and_b32_e32 v107, 0xffff0000, v107
	v_pk_fma_f32 v[96:97], v[100:101], s[30:31], v[96:97] op_sel_hi:[1,0,1]
	v_pk_fma_f32 v[94:95], v[110:111], s[30:31], v[94:95] op_sel_hi:[1,0,1]
	v_pk_fma_f32 v[92:93], v[102:103], s[30:31], v[92:93] op_sel_hi:[1,0,1]
	v_pk_fma_f32 v[90:91], v[112:113], s[30:31], v[90:91] op_sel_hi:[1,0,1]
	v_pk_fma_f32 v[100:101], v[104:105], s[30:31], v[88:89] op_sel_hi:[1,0,1]
	v_pk_fma_f32 v[102:103], v[114:115], s[30:31], v[86:87] op_sel_hi:[1,0,1]
; __device__ __forceinline__ unsigned cvt_pk_bf16(float lo, float hi) { const f32x2 v = {lo, hi}; return __builtin_bit_cast(unsigned, __builtin_convertvector(v, bf16x2_t)); }
; __device__ __forceinline__ float bflo(unsigned w) { return __uint_as_float(w << 16); }
; __device__ __forceinline__ float bfhi(unsigned w) { return __uint_as_float(w & 0xffff0000u); }
;     __device__ __forceinline__ void operator()(Acc& acc, const GUnit& u, int wr, int wc, int fr, int fq, LAS unsigned char*, int, int) const {
;     ...
;             for (int m = 0; m < 4; ++m) { const int row = row0 + ai * HALF + m * 16; float ps = 0.f, pq = 0.f;
; #pragma unroll
;                 for (int bj = 0; bj < 2; ++bj) { const size_t o = (size_t)row * DM + col0 + bj * HALF; const u32x4 hw = *(const u32x4*)(h0b + o);
;                     const f32x4 s0 = (f32x4){bflo(hw.x), bfhi(hw.x), bflo(hw.y), bfhi(hw.y)} * ALPHA + acc[ai][bj][m][0], s1 = (f32x4){bflo(hw.z), bfhi(hw.z), bflo(hw.w), bfhi(hw.w)} * ALPHA + acc[ai][bj][m][1];
;                     ps += ((s0[0] + s0[1]) + (s0[2] + s0[3])) + ((s1[0] + s1[1]) + (s1[2] + s1[3]));
;                     pq += ((s0[0] * s0[0] + s0[1] * s0[1]) + (s0[2] * s0[2] + s0[3] * s0[3])) + ((s1[0] * s1[0] + s1[1] * s1[1]) + (s1[2] * s1[2] + s1[3] * s1[3]));
;                     u32x4 w; w.x = cvt_pk_bf16(s0[0], s0[1]); w.y = cvt_pk_bf16(s0[2], s0[3]); w.z = cvt_pk_bf16(s1[0], s1[1]); w.w = cvt_pk_bf16(s1[2], s1[3]); *(u32x4*)(S + o) = w; }
;                 ps = xrow_sum(ps); pq = xrow_sum(pq);
;                 if (fq == 0) *(f32x2*)(part + ((size_t)row * 32 + u.pn * 4 + wc) * 2) = (f32x2){ps, pq}; }
	v_pk_fma_f32 v[104:105], v[106:107], s[30:31], v[84:85] op_sel_hi:[1,0,1]
	v_pk_fma_f32 v[106:107], v[116:117], s[30:31], v[82:83] op_sel_hi:[1,0,1]
	v_add_f32_e32 v110, v94, v95
	v_add_f32_e32 v111, v96, v97
	v_add_f32_e32 v112, v90, v91
	v_add_f32_e32 v113, v92, v93
	v_mul_f32_e32 v114, v95, v95
	v_mul_f32_e32 v115, v97, v97
	v_mul_f32_e32 v116, v91, v91
	v_mul_f32_e32 v117, v93, v93
	v_cvt_pk_bf16_f32 v82, v94, v95
	v_cvt_pk_bf16_f32 v83, v96, v97
	v_cvt_pk_bf16_f32 v84, v90, v91
	v_cvt_pk_bf16_f32 v85, v92, v93
	v_add_f32_e32 v91, v102, v103
	v_add_f32_e32 v93, v100, v101
	v_add_f32_e32 v95, v106, v107
	v_add_f32_e32 v97, v104, v105
	v_mul_f32_e32 v118, v103, v103
	v_mul_f32_e32 v119, v101, v101
	v_mul_f32_e32 v120, v107, v107
	v_mul_f32_e32 v121, v105, v105
	v_cvt_pk_bf16_f32 v86, v102, v103
	v_cvt_pk_bf16_f32 v87, v100, v101
	v_cvt_pk_bf16_f32 v88, v106, v107
	v_cvt_pk_bf16_f32 v89, v104, v105
	v_add_f32_e32 v101, v110, v111
	v_add_f32_e32 v103, v112, v113
	v_fmac_f32_e32 v114, v94, v94
	v_fmac_f32_e32 v115, v96, v96
	v_fmac_f32_e32 v116, v90, v90
	v_fmac_f32_e32 v117, v92, v92
	global_store_dwordx4 v[108:109], v[82:85], off
	v_fmac_f32_e32 v118, v102, v102
	v_fmac_f32_e32 v119, v100, v100
	v_add_f32_e32 v82, v91, v93
	v_add_f32_e32 v83, v95, v97
	v_fmac_f32_e32 v120, v106, v106
	v_fmac_f32_e32 v121, v104, v104
	global_store_dwordx4 v[108:109], v[86:89], off offset:256
	v_add_f32_e32 v84, v101, v103
	v_add_f32_e32 v85, v114, v115
	v_add_f32_e32 v86, v116, v117
	v_add_f32_e32 v82, v82, v83
	v_add_f32_e32 v83, v118, v119
	v_add_f32_e32 v87, v120, v121
	v_add_f32_e32 v84, 0, v84
	v_add_f32_e32 v85, v85, v86
	v_add_f32_e32 v83, v83, v87
	v_add_f32_e32 v82, v84, v82
	v_add_f32_e32 v83, v85, v83
	v_mov_b32_e32 v84, v82
	v_mov_b32_e32 v85, v83
	s_nop 0
	v_permlane16_swap_b32_e32 v82, v84
	v_permlane16_swap_b32_e32 v83, v85
	v_add_f32_e32 v82, v82, v84
	v_add_f32_e32 v83, v83, v85
	v_mov_b32_e32 v84, v82
	v_mov_b32_e32 v85, v83
	s_nop 0
	v_permlane32_swap_b32_e32 v82, v84
	v_permlane32_swap_b32_e32 v83, v85
	s_and_saveexec_b64 s[40:41], s[10:11]
	s_cbranch_execz .LBB0_839
	s_lshl_b32 s42, s4, 2
	v_pk_add_f32 v[82:83], v[82:83], v[84:85]
	v_lshlrev_b64 v[84:85], 5, v[98:99]
	s_ashr_i32 s43, s42, 31
	v_lshl_add_u64 v[84:85], v[84:85], 0, s[42:43]
	v_or_b32_e32 v84, s33, v84
	v_lshl_add_u64 v[84:85], v[84:85], 3, s[20:21]
	global_store_dwordx2 v[84:85], v[82:83], off
.LBB0_839:
	s_or_b64 exec, exec, s[40:41]
	v_add_u32_e32 v82, 48, v148
	v_ashrrev_i32_e32 v83, 31, v82
	v_lshlrev_b64 v[84:85], 11, v[82:83]
	v_lshl_add_u64 v[84:85], v[84:85], 0, v[146:147]
	v_lshlrev_b64 v[92:93], 1, v[84:85]
	v_lshl_add_u64 v[88:89], s[18:19], 0, v[92:93]
	v_mov_b32_e32 v84, v200
	v_mov_b32_e32 v85, v201
	v_mov_b32_e32 v86, v202
	v_mov_b32_e32 v87, v203
	s_nop 0
	v_mov_b32_e32 v88, v204
	v_mov_b32_e32 v89, v205
	v_mov_b32_e32 v90, v206
	v_mov_b32_e32 v91, v207
	v_lshl_add_u64 v[92:93], s[16:17], 0, v[92:93]
	v_lshlrev_b32_e32 v94, 16, v84
	v_and_b32_e32 v95, 0xffff0000, v84
	v_lshlrev_b32_e32 v84, 16, v85
	v_and_b32_e32 v85, 0xffff0000, v85
	v_lshlrev_b32_e32 v96, 16, v86
	v_and_b32_e32 v97, 0xffff0000, v86
	v_lshlrev_b32_e32 v86, 16, v87
	v_and_b32_e32 v87, 0xffff0000, v87
	v_lshlrev_b32_e32 v98, 16, v88
	v_and_b32_e32 v99, 0xffff0000, v88
	v_lshlrev_b32_e32 v88, 16, v89
	v_and_b32_e32 v89, 0xffff0000, v89
	v_lshlrev_b32_e32 v100, 16, v90
	v_and_b32_e32 v101, 0xffff0000, v90
	v_lshlrev_b32_e32 v90, 16, v91
	v_and_b32_e32 v91, 0xffff0000, v91
	v_pk_fma_f32 v[80:81], v[84:85], s[30:31], v[80:81] op_sel_hi:[1,0,1]
	v_pk_fma_f32 v[78:79], v[94:95], s[30:31], v[78:79] op_sel_hi:[1,0,1]
	v_pk_fma_f32 v[76:77], v[86:87], s[30:31], v[76:77] op_sel_hi:[1,0,1]
	v_pk_fma_f32 v[74:75], v[96:97], s[30:31], v[74:75] op_sel_hi:[1,0,1]
	v_pk_fma_f32 v[84:85], v[88:89], s[30:31], v[72:73] op_sel_hi:[1,0,1]
	v_pk_fma_f32 v[86:87], v[98:99], s[30:31], v[70:71] op_sel_hi:[1,0,1]
	v_pk_fma_f32 v[88:89], v[90:91], s[30:31], v[68:69] op_sel_hi:[1,0,1]
	v_pk_fma_f32 v[90:91], v[100:101], s[30:31], v[66:67] op_sel_hi:[1,0,1]
	v_add_f32_e32 v94, v78, v79
	v_add_f32_e32 v95, v80, v81
	v_add_f32_e32 v96, v74, v75
	v_add_f32_e32 v97, v76, v77
	v_mul_f32_e32 v98, v79, v79
	v_mul_f32_e32 v99, v81, v81
	v_mul_f32_e32 v100, v75, v75
	v_mul_f32_e32 v101, v77, v77
	v_cvt_pk_bf16_f32 v66, v78, v79
	v_cvt_pk_bf16_f32 v67, v80, v81
	v_cvt_pk_bf16_f32 v68, v74, v75
	v_cvt_pk_bf16_f32 v69, v76, v77
	v_add_f32_e32 v75, v86, v87
	v_add_f32_e32 v77, v84, v85
	v_add_f32_e32 v79, v90, v91
	v_add_f32_e32 v81, v88, v89
	v_mul_f32_e32 v102, v87, v87
	v_mul_f32_e32 v103, v85, v85
	v_mul_f32_e32 v104, v91, v91
	v_mul_f32_e32 v105, v89, v89
	v_cvt_pk_bf16_f32 v70, v86, v87
	v_cvt_pk_bf16_f32 v71, v84, v85
	v_cvt_pk_bf16_f32 v72, v90, v91
	v_cvt_pk_bf16_f32 v73, v88, v89
	v_add_f32_e32 v85, v94, v95
	v_add_f32_e32 v87, v96, v97
	v_fmac_f32_e32 v98, v78, v78
	v_fmac_f32_e32 v99, v80, v80
	v_fmac_f32_e32 v100, v74, v74
	v_fmac_f32_e32 v101, v76, v76
	global_store_dwordx4 v[92:93], v[66:69], off
	v_fmac_f32_e32 v102, v86, v86
	v_fmac_f32_e32 v103, v84, v84
	v_add_f32_e32 v66, v75, v77
	v_add_f32_e32 v67, v79, v81
	v_fmac_f32_e32 v104, v90, v90
	v_fmac_f32_e32 v105, v88, v88
	global_store_dwordx4 v[92:93], v[70:73], off offset:256
	v_add_f32_e32 v68, v85, v87
	v_add_f32_e32 v69, v98, v99
	v_add_f32_e32 v70, v100, v101
	v_add_f32_e32 v66, v66, v67
	v_add_f32_e32 v67, v102, v103
	v_add_f32_e32 v71, v104, v105
	v_add_f32_e32 v68, 0, v68
	v_add_f32_e32 v69, v69, v70
	v_add_f32_e32 v67, v67, v71
	v_add_f32_e32 v66, v68, v66
	v_add_f32_e32 v67, v69, v67
	v_mov_b32_e32 v68, v66
	v_mov_b32_e32 v69, v67
	s_nop 0
	v_permlane16_swap_b32_e32 v66, v68
	v_permlane16_swap_b32_e32 v67, v69
	v_add_f32_e32 v66, v66, v68
	v_add_f32_e32 v67, v67, v69
	v_mov_b32_e32 v68, v66
	v_mov_b32_e32 v69, v67
	s_nop 0
	v_permlane32_swap_b32_e32 v66, v68
	v_permlane32_swap_b32_e32 v67, v69
	s_and_saveexec_b64 s[40:41], s[10:11]
	s_cbranch_execz .LBB0_841
	s_lshl_b32 s42, s4, 2
	v_pk_add_f32 v[66:67], v[66:67], v[68:69]
	v_lshlrev_b64 v[68:69], 5, v[82:83]
	s_ashr_i32 s43, s42, 31
	v_lshl_add_u64 v[68:69], v[68:69], 0, s[42:43]
	v_or_b32_e32 v68, s33, v68
	v_lshl_add_u64 v[68:69], v[68:69], 3, s[20:21]
	global_store_dwordx2 v[68:69], v[66:67], off
; __device__ __forceinline__ unsigned cvt_pk_bf16(float lo, float hi) { const f32x2 v = {lo, hi}; return __builtin_bit_cast(unsigned, __builtin_convertvector(v, bf16x2_t)); }
; __device__ __forceinline__ float bflo(unsigned w) { return __uint_as_float(w << 16); }
; __device__ __forceinline__ float bfhi(unsigned w) { return __uint_as_float(w & 0xffff0000u); }
;     __device__ __forceinline__ void operator()(Acc& acc, const GUnit& u, int wr, int wc, int fr, int fq, LAS unsigned char*, int, int) const {
;     ...
;             for (int m = 0; m < 4; ++m) { const int row = row0 + ai * HALF + m * 16; float ps = 0.f, pq = 0.f;
; #pragma unroll
;                 for (int bj = 0; bj < 2; ++bj) { const size_t o = (size_t)row * DM + col0 + bj * HALF; const u32x4 hw = *(const u32x4*)(h0b + o);
;                     const f32x4 s0 = (f32x4){bflo(hw.x), bfhi(hw.x), bflo(hw.y), bfhi(hw.y)} * ALPHA + acc[ai][bj][m][0], s1 = (f32x4){bflo(hw.z), bfhi(hw.z), bflo(hw.w), bfhi(hw.w)} * ALPHA + acc[ai][bj][m][1];
;                     ps += ((s0[0] + s0[1]) + (s0[2] + s0[3])) + ((s1[0] + s1[1]) + (s1[2] + s1[3]));
;                     pq += ((s0[0] * s0[0] + s0[1] * s0[1]) + (s0[2] * s0[2] + s0[3] * s0[3])) + ((s1[0] * s1[0] + s1[1] * s1[1]) + (s1[2] * s1[2] + s1[3] * s1[3]));
;                     u32x4 w; w.x = cvt_pk_bf16(s0[0], s0[1]); w.y = cvt_pk_bf16(s0[2], s0[3]); w.z = cvt_pk_bf16(s1[0], s1[1]); w.w = cvt_pk_bf16(s1[2], s1[3]); *(u32x4*)(S + o) = w; }
;                 ps = xrow_sum(ps); pq = xrow_sum(pq);
;                 if (fq == 0) *(f32x2*)(part + ((size_t)row * 32 + u.pn * 4 + wc) * 2) = (f32x2){ps, pq}; }
.LBB0_841:
	s_or_b64 exec, exec, s[40:41]
	v_add_u32_e32 v66, 0x80, v148
	v_ashrrev_i32_e32 v67, 31, v66
	v_lshlrev_b64 v[68:69], 11, v[66:67]
	v_lshl_add_u64 v[68:69], v[68:69], 0, v[146:147]
	v_lshlrev_b64 v[76:77], 1, v[68:69]
	v_lshl_add_u64 v[72:73], s[18:19], 0, v[76:77]
	v_mov_b32_e32 v68, v208
	v_mov_b32_e32 v69, v209
	v_mov_b32_e32 v70, v210
	v_mov_b32_e32 v71, v211
	s_nop 0
	v_mov_b32_e32 v72, v212
	v_mov_b32_e32 v73, v213
	v_mov_b32_e32 v74, v214
	v_mov_b32_e32 v75, v215
	v_lshl_add_u64 v[76:77], s[16:17], 0, v[76:77]
	v_lshlrev_b32_e32 v78, 16, v68
	v_and_b32_e32 v79, 0xffff0000, v68
	v_lshlrev_b32_e32 v68, 16, v69
	v_and_b32_e32 v69, 0xffff0000, v69
	v_lshlrev_b32_e32 v80, 16, v70
	v_and_b32_e32 v81, 0xffff0000, v70
	v_lshlrev_b32_e32 v70, 16, v71
	v_and_b32_e32 v71, 0xffff0000, v71
	v_lshlrev_b32_e32 v82, 16, v72
	v_and_b32_e32 v83, 0xffff0000, v72
	v_lshlrev_b32_e32 v72, 16, v73
	v_and_b32_e32 v73, 0xffff0000, v73
	v_lshlrev_b32_e32 v84, 16, v74
	v_and_b32_e32 v85, 0xffff0000, v74
	v_lshlrev_b32_e32 v74, 16, v75
	v_and_b32_e32 v75, 0xffff0000, v75
	v_pk_fma_f32 v[64:65], v[68:69], s[30:31], v[64:65] op_sel_hi:[1,0,1]
	v_pk_fma_f32 v[62:63], v[78:79], s[30:31], v[62:63] op_sel_hi:[1,0,1]
	v_pk_fma_f32 v[60:61], v[70:71], s[30:31], v[60:61] op_sel_hi:[1,0,1]
	v_pk_fma_f32 v[58:59], v[80:81], s[30:31], v[58:59] op_sel_hi:[1,0,1]
	v_pk_fma_f32 v[68:69], v[72:73], s[30:31], v[56:57] op_sel_hi:[1,0,1]
	v_pk_fma_f32 v[70:71], v[82:83], s[30:31], v[54:55] op_sel_hi:[1,0,1]
	v_pk_fma_f32 v[72:73], v[74:75], s[30:31], v[52:53] op_sel_hi:[1,0,1]
	v_pk_fma_f32 v[74:75], v[84:85], s[30:31], v[50:51] op_sel_hi:[1,0,1]
	v_add_f32_e32 v78, v62, v63
	v_add_f32_e32 v79, v64, v65
	v_add_f32_e32 v80, v58, v59
	v_add_f32_e32 v81, v60, v61
	v_mul_f32_e32 v82, v63, v63
	v_mul_f32_e32 v83, v65, v65
	v_mul_f32_e32 v84, v59, v59
	v_mul_f32_e32 v85, v61, v61
	v_cvt_pk_bf16_f32 v50, v62, v63
	v_cvt_pk_bf16_f32 v51, v64, v65
	v_cvt_pk_bf16_f32 v52, v58, v59
	v_cvt_pk_bf16_f32 v53, v60, v61
	v_add_f32_e32 v59, v70, v71
	v_add_f32_e32 v61, v68, v69
	v_add_f32_e32 v63, v74, v75
	v_add_f32_e32 v65, v72, v73
	v_mul_f32_e32 v86, v71, v71
	v_mul_f32_e32 v87, v69, v69
	v_mul_f32_e32 v88, v75, v75
	v_mul_f32_e32 v89, v73, v73
	v_cvt_pk_bf16_f32 v54, v70, v71
	v_cvt_pk_bf16_f32 v55, v68, v69
	v_cvt_pk_bf16_f32 v56, v74, v75
	v_cvt_pk_bf16_f32 v57, v72, v73
	v_add_f32_e32 v69, v78, v79
	v_add_f32_e32 v71, v80, v81
	v_fmac_f32_e32 v82, v62, v62
	v_fmac_f32_e32 v83, v64, v64
	v_fmac_f32_e32 v84, v58, v58
	v_fmac_f32_e32 v85, v60, v60
	global_store_dwordx4 v[76:77], v[50:53], off
	v_fmac_f32_e32 v86, v70, v70
	v_fmac_f32_e32 v87, v68, v68
	v_add_f32_e32 v50, v59, v61
	v_add_f32_e32 v51, v63, v65
	v_fmac_f32_e32 v88, v74, v74
	v_fmac_f32_e32 v89, v72, v72
	global_store_dwordx4 v[76:77], v[54:57], off offset:256
	v_add_f32_e32 v52, v69, v71
	v_add_f32_e32 v53, v82, v83
	v_add_f32_e32 v54, v84, v85
	v_add_f32_e32 v50, v50, v51
	v_add_f32_e32 v51, v86, v87
	v_add_f32_e32 v55, v88, v89
	v_add_f32_e32 v52, 0, v52
	v_add_f32_e32 v53, v53, v54
	v_add_f32_e32 v51, v51, v55
	v_add_f32_e32 v50, v52, v50
	v_add_f32_e32 v51, v53, v51
	v_mov_b32_e32 v52, v50
	v_mov_b32_e32 v53, v51
	s_nop 0
	v_permlane16_swap_b32_e32 v50, v52
	v_permlane16_swap_b32_e32 v51, v53
	v_add_f32_e32 v50, v50, v52
	v_add_f32_e32 v51, v51, v53
	v_mov_b32_e32 v52, v50
	v_mov_b32_e32 v53, v51
	s_nop 0
	v_permlane32_swap_b32_e32 v50, v52
	v_permlane32_swap_b32_e32 v51, v53
	s_and_saveexec_b64 s[40:41], s[10:11]
	s_cbranch_execz .LBB0_843
	s_lshl_b32 s42, s4, 2
	v_pk_add_f32 v[50:51], v[50:51], v[52:53]
	v_lshlrev_b64 v[52:53], 5, v[66:67]
	s_ashr_i32 s43, s42, 31
	v_lshl_add_u64 v[52:53], v[52:53], 0, s[42:43]
	v_or_b32_e32 v52, s33, v52
	v_lshl_add_u64 v[52:53], v[52:53], 3, s[20:21]
	global_store_dwordx2 v[52:53], v[50:51], off
.LBB0_843:
	s_or_b64 exec, exec, s[40:41]
	v_add_u32_e32 v50, 0x90, v148
	v_ashrrev_i32_e32 v51, 31, v50
	v_lshlrev_b64 v[52:53], 11, v[50:51]
	v_lshl_add_u64 v[52:53], v[52:53], 0, v[146:147]
	v_lshlrev_b64 v[60:61], 1, v[52:53]
	v_lshl_add_u64 v[56:57], s[18:19], 0, v[60:61]
	v_mov_b32_e32 v52, v216
	v_mov_b32_e32 v53, v217
	v_mov_b32_e32 v54, v218
	v_mov_b32_e32 v55, v219
	s_nop 0
	v_mov_b32_e32 v56, v220
	v_mov_b32_e32 v57, v221
	v_mov_b32_e32 v58, v222
	v_mov_b32_e32 v59, v223
	v_lshl_add_u64 v[60:61], s[16:17], 0, v[60:61]
	v_lshlrev_b32_e32 v62, 16, v52
	v_and_b32_e32 v63, 0xffff0000, v52
	v_lshlrev_b32_e32 v52, 16, v53
	v_and_b32_e32 v53, 0xffff0000, v53
	v_lshlrev_b32_e32 v64, 16, v54
	v_and_b32_e32 v65, 0xffff0000, v54
	v_lshlrev_b32_e32 v54, 16, v55
	v_and_b32_e32 v55, 0xffff0000, v55
	v_lshlrev_b32_e32 v66, 16, v56
	v_and_b32_e32 v67, 0xffff0000, v56
	v_lshlrev_b32_e32 v56, 16, v57
	v_and_b32_e32 v57, 0xffff0000, v57
	v_lshlrev_b32_e32 v68, 16, v58
	v_and_b32_e32 v69, 0xffff0000, v58
	v_lshlrev_b32_e32 v58, 16, v59
	v_and_b32_e32 v59, 0xffff0000, v59
	v_pk_fma_f32 v[48:49], v[52:53], s[30:31], v[48:49] op_sel_hi:[1,0,1]
	v_pk_fma_f32 v[46:47], v[62:63], s[30:31], v[46:47] op_sel_hi:[1,0,1]
	v_pk_fma_f32 v[44:45], v[54:55], s[30:31], v[44:45] op_sel_hi:[1,0,1]
	v_pk_fma_f32 v[42:43], v[64:65], s[30:31], v[42:43] op_sel_hi:[1,0,1]
	v_pk_fma_f32 v[52:53], v[56:57], s[30:31], v[40:41] op_sel_hi:[1,0,1]
	v_pk_fma_f32 v[54:55], v[66:67], s[30:31], v[38:39] op_sel_hi:[1,0,1]
	v_pk_fma_f32 v[56:57], v[58:59], s[30:31], v[36:37] op_sel_hi:[1,0,1]
	v_pk_fma_f32 v[58:59], v[68:69], s[30:31], v[34:35] op_sel_hi:[1,0,1]
	v_add_f32_e32 v62, v46, v47
	v_add_f32_e32 v63, v48, v49
	v_add_f32_e32 v64, v42, v43
	v_add_f32_e32 v65, v44, v45
	v_mul_f32_e32 v66, v47, v47
	v_mul_f32_e32 v67, v49, v49
; __device__ __forceinline__ unsigned cvt_pk_bf16(float lo, float hi) { const f32x2 v = {lo, hi}; return __builtin_bit_cast(unsigned, __builtin_convertvector(v, bf16x2_t)); }
; __device__ __forceinline__ float bflo(unsigned w) { return __uint_as_float(w << 16); }
; __device__ __forceinline__ float bfhi(unsigned w) { return __uint_as_float(w & 0xffff0000u); }
;     __device__ __forceinline__ void operator()(Acc& acc, const GUnit& u, int wr, int wc, int fr, int fq, LAS unsigned char*, int, int) const {
;     ...
;             for (int m = 0; m < 4; ++m) { const int row = row0 + ai * HALF + m * 16; float ps = 0.f, pq = 0.f;
; #pragma unroll
;                 for (int bj = 0; bj < 2; ++bj) { const size_t o = (size_t)row * DM + col0 + bj * HALF; const u32x4 hw = *(const u32x4*)(h0b + o);
;                     const f32x4 s0 = (f32x4){bflo(hw.x), bfhi(hw.x), bflo(hw.y), bfhi(hw.y)} * ALPHA + acc[ai][bj][m][0], s1 = (f32x4){bflo(hw.z), bfhi(hw.z), bflo(hw.w), bfhi(hw.w)} * ALPHA + acc[ai][bj][m][1];
;                     ps += ((s0[0] + s0[1]) + (s0[2] + s0[3])) + ((s1[0] + s1[1]) + (s1[2] + s1[3]));
;                     pq += ((s0[0] * s0[0] + s0[1] * s0[1]) + (s0[2] * s0[2] + s0[3] * s0[3])) + ((s1[0] * s1[0] + s1[1] * s1[1]) + (s1[2] * s1[2] + s1[3] * s1[3]));
;                     u32x4 w; w.x = cvt_pk_bf16(s0[0], s0[1]); w.y = cvt_pk_bf16(s0[2], s0[3]); w.z = cvt_pk_bf16(s1[0], s1[1]); w.w = cvt_pk_bf16(s1[2], s1[3]); *(u32x4*)(S + o) = w; }
;                 ps = xrow_sum(ps); pq = xrow_sum(pq);
;                 if (fq == 0) *(f32x2*)(part + ((size_t)row * 32 + u.pn * 4 + wc) * 2) = (f32x2){ps, pq}; }
	v_mul_f32_e32 v68, v43, v43
	v_mul_f32_e32 v69, v45, v45
	v_cvt_pk_bf16_f32 v34, v46, v47
	v_cvt_pk_bf16_f32 v35, v48, v49
	v_cvt_pk_bf16_f32 v36, v42, v43
	v_cvt_pk_bf16_f32 v37, v44, v45
	v_add_f32_e32 v43, v54, v55
	v_add_f32_e32 v45, v52, v53
	v_add_f32_e32 v47, v58, v59
	v_add_f32_e32 v49, v56, v57
	v_mul_f32_e32 v70, v55, v55
	v_mul_f32_e32 v71, v53, v53
	v_mul_f32_e32 v72, v59, v59
	v_mul_f32_e32 v73, v57, v57
	v_cvt_pk_bf16_f32 v38, v54, v55
	v_cvt_pk_bf16_f32 v39, v52, v53
	v_cvt_pk_bf16_f32 v40, v58, v59
	v_cvt_pk_bf16_f32 v41, v56, v57
	v_add_f32_e32 v53, v62, v63
	v_add_f32_e32 v55, v64, v65
	v_fmac_f32_e32 v66, v46, v46
	v_fmac_f32_e32 v67, v48, v48
	v_fmac_f32_e32 v68, v42, v42
	v_fmac_f32_e32 v69, v44, v44
	global_store_dwordx4 v[60:61], v[34:37], off
	v_fmac_f32_e32 v70, v54, v54
	v_fmac_f32_e32 v71, v52, v52
	v_add_f32_e32 v34, v43, v45
	v_add_f32_e32 v35, v47, v49
	v_fmac_f32_e32 v72, v58, v58
	v_fmac_f32_e32 v73, v56, v56
	global_store_dwordx4 v[60:61], v[38:41], off offset:256
	v_add_f32_e32 v36, v53, v55
	v_add_f32_e32 v37, v66, v67
	v_add_f32_e32 v38, v68, v69
	v_add_f32_e32 v34, v34, v35
	v_add_f32_e32 v35, v70, v71
	v_add_f32_e32 v39, v72, v73
	v_add_f32_e32 v36, 0, v36
	v_add_f32_e32 v37, v37, v38
	v_add_f32_e32 v35, v35, v39
	v_add_f32_e32 v34, v36, v34
	v_add_f32_e32 v35, v37, v35
	v_mov_b32_e32 v36, v34
	v_mov_b32_e32 v37, v35
	s_nop 0
	v_permlane16_swap_b32_e32 v34, v36
	v_permlane16_swap_b32_e32 v35, v37
	v_add_f32_e32 v34, v34, v36
	v_add_f32_e32 v35, v35, v37
	v_mov_b32_e32 v36, v34
	v_mov_b32_e32 v37, v35
	s_nop 0
	v_permlane32_swap_b32_e32 v34, v36
	v_permlane32_swap_b32_e32 v35, v37
	s_and_saveexec_b64 s[40:41], s[10:11]
	s_cbranch_execz .LBB0_845
	s_lshl_b32 s42, s4, 2
	v_pk_add_f32 v[34:35], v[34:35], v[36:37]
	v_lshlrev_b64 v[36:37], 5, v[50:51]
	s_ashr_i32 s43, s42, 31
	v_lshl_add_u64 v[36:37], v[36:37], 0, s[42:43]
	v_or_b32_e32 v36, s33, v36
	v_lshl_add_u64 v[36:37], v[36:37], 3, s[20:21]
	global_store_dwordx2 v[36:37], v[34:35], off
.LBB0_845:
	s_or_b64 exec, exec, s[40:41]
	v_add_u32_e32 v34, 0xa0, v148
	v_ashrrev_i32_e32 v35, 31, v34
	v_lshlrev_b64 v[36:37], 11, v[34:35]
	v_lshl_add_u64 v[36:37], v[36:37], 0, v[146:147]
	v_lshlrev_b64 v[44:45], 1, v[36:37]
	v_lshl_add_u64 v[40:41], s[18:19], 0, v[44:45]
	v_mov_b32_e32 v36, v224
	v_mov_b32_e32 v37, v225
	v_mov_b32_e32 v38, v226
	v_mov_b32_e32 v39, v227
	s_nop 0
	v_mov_b32_e32 v40, v228
	v_mov_b32_e32 v41, v229
	v_mov_b32_e32 v42, v230
	v_mov_b32_e32 v43, v231
	v_lshl_add_u64 v[44:45], s[16:17], 0, v[44:45]
	v_lshlrev_b32_e32 v46, 16, v36
	v_and_b32_e32 v47, 0xffff0000, v36
	v_lshlrev_b32_e32 v36, 16, v37
	v_and_b32_e32 v37, 0xffff0000, v37
	v_lshlrev_b32_e32 v48, 16, v38
	v_and_b32_e32 v49, 0xffff0000, v38
	v_lshlrev_b32_e32 v38, 16, v39
	v_and_b32_e32 v39, 0xffff0000, v39
	v_lshlrev_b32_e32 v50, 16, v40
	v_and_b32_e32 v51, 0xffff0000, v40
	v_lshlrev_b32_e32 v40, 16, v41
	v_and_b32_e32 v41, 0xffff0000, v41
	v_lshlrev_b32_e32 v52, 16, v42
	v_and_b32_e32 v53, 0xffff0000, v42
	v_lshlrev_b32_e32 v42, 16, v43
	v_and_b32_e32 v43, 0xffff0000, v43
	v_pk_fma_f32 v[32:33], v[36:37], s[30:31], v[32:33] op_sel_hi:[1,0,1]
	v_pk_fma_f32 v[30:31], v[46:47], s[30:31], v[30:31] op_sel_hi:[1,0,1]
	v_pk_fma_f32 v[28:29], v[38:39], s[30:31], v[28:29] op_sel_hi:[1,0,1]
	v_pk_fma_f32 v[26:27], v[48:49], s[30:31], v[26:27] op_sel_hi:[1,0,1]
	v_pk_fma_f32 v[36:37], v[40:41], s[30:31], v[24:25] op_sel_hi:[1,0,1]
	v_pk_fma_f32 v[38:39], v[50:51], s[30:31], v[22:23] op_sel_hi:[1,0,1]
	v_pk_fma_f32 v[40:41], v[42:43], s[30:31], v[20:21] op_sel_hi:[1,0,1]
	v_pk_fma_f32 v[42:43], v[52:53], s[30:31], v[18:19] op_sel_hi:[1,0,1]
	v_add_f32_e32 v46, v30, v31
	v_add_f32_e32 v47, v32, v33
	v_add_f32_e32 v48, v26, v27
	v_add_f32_e32 v49, v28, v29
	v_mul_f32_e32 v50, v31, v31
	v_mul_f32_e32 v51, v33, v33
	v_mul_f32_e32 v52, v27, v27
	v_mul_f32_e32 v53, v29, v29
	v_cvt_pk_bf16_f32 v18, v30, v31
	v_cvt_pk_bf16_f32 v19, v32, v33
	v_cvt_pk_bf16_f32 v20, v26, v27
	v_cvt_pk_bf16_f32 v21, v28, v29
	v_add_f32_e32 v27, v38, v39
	v_add_f32_e32 v29, v36, v37
	v_add_f32_e32 v31, v42, v43
	v_add_f32_e32 v33, v40, v41
	v_mul_f32_e32 v54, v39, v39
	v_mul_f32_e32 v55, v37, v37
	v_mul_f32_e32 v56, v43, v43
	v_mul_f32_e32 v57, v41, v41
	v_cvt_pk_bf16_f32 v22, v38, v39
	v_cvt_pk_bf16_f32 v23, v36, v37
	v_cvt_pk_bf16_f32 v24, v42, v43
	v_cvt_pk_bf16_f32 v25, v40, v41
	v_add_f32_e32 v37, v46, v47
	v_add_f32_e32 v39, v48, v49
	v_fmac_f32_e32 v50, v30, v30
	v_fmac_f32_e32 v51, v32, v32
	v_fmac_f32_e32 v52, v26, v26
	v_fmac_f32_e32 v53, v28, v28
	global_store_dwordx4 v[44:45], v[18:21], off
	v_fmac_f32_e32 v54, v38, v38
	v_fmac_f32_e32 v55, v36, v36
	v_add_f32_e32 v18, v27, v29
	v_add_f32_e32 v19, v31, v33
	v_fmac_f32_e32 v56, v42, v42
	v_fmac_f32_e32 v57, v40, v40
	global_store_dwordx4 v[44:45], v[22:25], off offset:256
	v_add_f32_e32 v20, v37, v39
	v_add_f32_e32 v21, v50, v51
	v_add_f32_e32 v22, v52, v53
	v_add_f32_e32 v18, v18, v19
	v_add_f32_e32 v19, v54, v55
	v_add_f32_e32 v23, v56, v57
	v_add_f32_e32 v20, 0, v20
	v_add_f32_e32 v21, v21, v22
	v_add_f32_e32 v19, v19, v23
	v_add_f32_e32 v18, v20, v18
	v_add_f32_e32 v19, v21, v19
	v_mov_b32_e32 v20, v18
	v_mov_b32_e32 v21, v19
	s_nop 0
	v_permlane16_swap_b32_e32 v18, v20
	v_permlane16_swap_b32_e32 v19, v21
	v_add_f32_e32 v18, v18, v20
	v_add_f32_e32 v19, v19, v21
	v_mov_b32_e32 v20, v18
	v_mov_b32_e32 v21, v19
	s_nop 0
	v_permlane32_swap_b32_e32 v18, v20
	v_permlane32_swap_b32_e32 v19, v21
	s_and_saveexec_b64 s[40:41], s[10:11]
	s_cbranch_execz .LBB0_847
	s_lshl_b32 s42, s4, 2
	v_pk_add_f32 v[18:19], v[18:19], v[20:21]
	v_lshlrev_b64 v[20:21], 5, v[34:35]
	s_ashr_i32 s43, s42, 31
	v_lshl_add_u64 v[20:21], v[20:21], 0, s[42:43]
	v_or_b32_e32 v20, s33, v20
	v_lshl_add_u64 v[20:21], v[20:21], 3, s[20:21]
	global_store_dwordx2 v[20:21], v[18:19], off
; __device__ __forceinline__ unsigned cvt_pk_bf16(float lo, float hi) { const f32x2 v = {lo, hi}; return __builtin_bit_cast(unsigned, __builtin_convertvector(v, bf16x2_t)); }
; __device__ __forceinline__ float bflo(unsigned w) { return __uint_as_float(w << 16); }
; __device__ __forceinline__ float bfhi(unsigned w) { return __uint_as_float(w & 0xffff0000u); }
;     __device__ __forceinline__ void operator()(Acc& acc, const GUnit& u, int wr, int wc, int fr, int fq, LAS unsigned char*, int, int) const {
;     ...
;             for (int m = 0; m < 4; ++m) { const int row = row0 + ai * HALF + m * 16; float ps = 0.f, pq = 0.f;
; #pragma unroll
;                 for (int bj = 0; bj < 2; ++bj) { const size_t o = (size_t)row * DM + col0 + bj * HALF; const u32x4 hw = *(const u32x4*)(h0b + o);
;                     const f32x4 s0 = (f32x4){bflo(hw.x), bfhi(hw.x), bflo(hw.y), bfhi(hw.y)} * ALPHA + acc[ai][bj][m][0], s1 = (f32x4){bflo(hw.z), bfhi(hw.z), bflo(hw.w), bfhi(hw.w)} * ALPHA + acc[ai][bj][m][1];
;                     ps += ((s0[0] + s0[1]) + (s0[2] + s0[3])) + ((s1[0] + s1[1]) + (s1[2] + s1[3]));
;                     pq += ((s0[0] * s0[0] + s0[1] * s0[1]) + (s0[2] * s0[2] + s0[3] * s0[3])) + ((s1[0] * s1[0] + s1[1] * s1[1]) + (s1[2] * s1[2] + s1[3] * s1[3]));
;                     u32x4 w; w.x = cvt_pk_bf16(s0[0], s0[1]); w.y = cvt_pk_bf16(s0[2], s0[3]); w.z = cvt_pk_bf16(s1[0], s1[1]); w.w = cvt_pk_bf16(s1[2], s1[3]); *(u32x4*)(S + o) = w; }
;                 ps = xrow_sum(ps); pq = xrow_sum(pq);
;                 if (fq == 0) *(f32x2*)(part + ((size_t)row * 32 + u.pn * 4 + wc) * 2) = (f32x2){ps, pq}; }
.LBB0_847:
	s_or_b64 exec, exec, s[40:41]
	v_add_u32_e32 v18, 0xb0, v148
	v_ashrrev_i32_e32 v19, 31, v18
	v_lshlrev_b64 v[20:21], 11, v[18:19]
	v_lshl_add_u64 v[20:21], v[20:21], 0, v[146:147]
	v_lshlrev_b64 v[28:29], 1, v[20:21]
	v_lshl_add_u64 v[24:25], s[18:19], 0, v[28:29]
	v_mov_b32_e32 v20, v232
	v_mov_b32_e32 v21, v233
	v_mov_b32_e32 v22, v234
	v_mov_b32_e32 v23, v235
	s_nop 0
	v_mov_b32_e32 v24, v236
	v_mov_b32_e32 v25, v237
	v_mov_b32_e32 v26, v238
	v_mov_b32_e32 v27, v239
	v_lshl_add_u64 v[28:29], s[16:17], 0, v[28:29]
	v_lshlrev_b32_e32 v30, 16, v20
	v_and_b32_e32 v31, 0xffff0000, v20
	v_lshlrev_b32_e32 v20, 16, v21
	v_and_b32_e32 v21, 0xffff0000, v21
	v_lshlrev_b32_e32 v32, 16, v22
	v_and_b32_e32 v33, 0xffff0000, v22
	v_lshlrev_b32_e32 v22, 16, v23
	v_and_b32_e32 v23, 0xffff0000, v23
	v_lshlrev_b32_e32 v34, 16, v24
	v_and_b32_e32 v35, 0xffff0000, v24
	v_lshlrev_b32_e32 v24, 16, v25
	v_and_b32_e32 v25, 0xffff0000, v25
	v_lshlrev_b32_e32 v36, 16, v26
	v_and_b32_e32 v37, 0xffff0000, v26
	v_lshlrev_b32_e32 v26, 16, v27
	v_and_b32_e32 v27, 0xffff0000, v27
	v_pk_fma_f32 v[16:17], v[20:21], s[30:31], v[16:17] op_sel_hi:[1,0,1]
	v_pk_fma_f32 v[14:15], v[30:31], s[30:31], v[14:15] op_sel_hi:[1,0,1]
	v_pk_fma_f32 v[12:13], v[22:23], s[30:31], v[12:13] op_sel_hi:[1,0,1]
	v_pk_fma_f32 v[10:11], v[32:33], s[30:31], v[10:11] op_sel_hi:[1,0,1]
	v_pk_fma_f32 v[20:21], v[24:25], s[30:31], v[8:9] op_sel_hi:[1,0,1]
	v_pk_fma_f32 v[22:23], v[34:35], s[30:31], v[6:7] op_sel_hi:[1,0,1]
	v_pk_fma_f32 v[24:25], v[26:27], s[30:31], v[4:5] op_sel_hi:[1,0,1]
	v_pk_fma_f32 v[26:27], v[36:37], s[30:31], v[2:3] op_sel_hi:[1,0,1]
	v_add_f32_e32 v30, v14, v15
	v_add_f32_e32 v31, v16, v17
	v_add_f32_e32 v32, v10, v11
	v_add_f32_e32 v33, v12, v13
	v_mul_f32_e32 v34, v15, v15
	v_mul_f32_e32 v35, v17, v17
	v_mul_f32_e32 v36, v11, v11
	v_mul_f32_e32 v37, v13, v13
	v_cvt_pk_bf16_f32 v2, v14, v15
	v_cvt_pk_bf16_f32 v3, v16, v17
	v_cvt_pk_bf16_f32 v4, v10, v11
	v_cvt_pk_bf16_f32 v5, v12, v13
	v_add_f32_e32 v11, v22, v23
	v_add_f32_e32 v13, v20, v21
	v_add_f32_e32 v15, v26, v27
	v_add_f32_e32 v17, v24, v25
	v_mul_f32_e32 v38, v23, v23
	v_mul_f32_e32 v39, v21, v21
	v_mul_f32_e32 v40, v27, v27
	v_mul_f32_e32 v41, v25, v25
	v_cvt_pk_bf16_f32 v6, v22, v23
	v_cvt_pk_bf16_f32 v7, v20, v21
	v_cvt_pk_bf16_f32 v8, v26, v27
	v_cvt_pk_bf16_f32 v9, v24, v25
	v_add_f32_e32 v21, v30, v31
	v_add_f32_e32 v23, v32, v33
	v_fmac_f32_e32 v34, v14, v14
	v_fmac_f32_e32 v35, v16, v16
	v_fmac_f32_e32 v36, v10, v10
	v_fmac_f32_e32 v37, v12, v12
	global_store_dwordx4 v[28:29], v[2:5], off
	v_fmac_f32_e32 v38, v22, v22
	v_fmac_f32_e32 v39, v20, v20
	v_add_f32_e32 v2, v11, v13
	v_add_f32_e32 v3, v15, v17
	v_fmac_f32_e32 v40, v26, v26
	v_fmac_f32_e32 v41, v24, v24
	global_store_dwordx4 v[28:29], v[6:9], off offset:256
	v_add_f32_e32 v4, v21, v23
	v_add_f32_e32 v5, v34, v35
	v_add_f32_e32 v6, v36, v37
	v_add_f32_e32 v2, v2, v3
	v_add_f32_e32 v3, v38, v39
	v_add_f32_e32 v7, v40, v41
	v_add_f32_e32 v4, 0, v4
	v_add_f32_e32 v5, v5, v6
	v_add_f32_e32 v3, v3, v7
	v_add_f32_e32 v2, v4, v2
	v_add_f32_e32 v3, v5, v3
	v_mov_b32_e32 v4, v2
	v_mov_b32_e32 v5, v3
	s_nop 0
	v_permlane16_swap_b32_e32 v2, v4
	v_permlane16_swap_b32_e32 v3, v5
	v_add_f32_e32 v2, v2, v4
	v_add_f32_e32 v3, v3, v5
	v_mov_b32_e32 v4, v2
	v_mov_b32_e32 v5, v3
	s_nop 0
	v_permlane32_swap_b32_e32 v2, v4
	v_permlane32_swap_b32_e32 v3, v5
	s_and_saveexec_b64 s[40:41], s[10:11]
	s_cbranch_execz .LBB0_849
	s_lshl_b32 s42, s4, 2
	v_pk_add_f32 v[2:3], v[2:3], v[4:5]
	v_lshlrev_b64 v[4:5], 5, v[18:19]
	s_ashr_i32 s43, s42, 31
	v_lshl_add_u64 v[4:5], v[4:5], 0, s[42:43]
	v_or_b32_e32 v4, s33, v4
	v_lshl_add_u64 v[4:5], v[4:5], 3, s[20:21]
	global_store_dwordx2 v[4:5], v[2:3], off

; __device__ __forceinline__ unsigned cvt_pk_bf16(float lo, float hi) { const f32x2 v = {lo, hi}; return __builtin_bit_cast(unsigned, __builtin_convertvector(v, bf16x2_t)); }
;     __device__ __forceinline__ void operator()(Acc& acc, const GUnit& u, int wr, int wc, int fr, int fq, LAS unsigned char*, int, int) const {
;         const int e = u.pm, j = u.x1 & 0xffff, n = cnt[e];
;         const int col0 = u.pn * 256 + wc * 32 + 8 * fq;
; #pragma unroll
;         for (int ai = 0; ai < 2; ++ai)
; #pragma unroll
;             for (int m = 0; m < 4; ++m) { const int idx = j * 256 + ai * HALF + wr * 64 + m * 16 + fr;
;                 if (idx < n) { const int dest = slot[(size_t)e * CAP + idx]; bf16_t* rowp = Y + (size_t)dest * 2048 + col0;
; #pragma unroll
;                     for (int bj = 0; bj < 2; ++bj) { const f32x4 v0 = acc[ai][bj][m][0], v1 = acc[ai][bj][m][1];
;                         u32x4 w; w.x = cvt_pk_bf16(v0[0], v0[1]); w.y = cvt_pk_bf16(v0[2], v0[3]); w.z = cvt_pk_bf16(v1[0], v1[1]); w.w = cvt_pk_bf16(v1[2], v1[3]);
;                         *(u32x4*)(rowp + bj * HALF) = w; } } }
.LBB0_1435:
	s_lshl_b32 s6, s28, 2
	s_add_i32 s6, s6, 0
	s_add_i32 s6, s6, 0x22200
	v_mov_b32_e32 v3, s6
	ds_read_b32 v3, v3
	s_lshl_b32 s6, s48, 8
	s_and_b32 s6, s6, 0xffff00
	s_ashr_i32 s29, s28, 31
	v_lshl_or_b32 v4, s47, 8, v217
	v_add_u32_e32 v134, s6, v1
	s_lshl_b64 s[6:7], s[28:29], 17
	v_ashrrev_i32_e32 v5, 31, v4
	s_waitcnt lgkmcnt(0)
	v_cmp_lt_i32_e32 vcc, v134, v3
	v_ashrrev_i32_e32 v135, 31, v134
	s_add_u32 s30, s27, s6
	s_addc_u32 s31, s33, s7
	v_lshl_add_u64 v[252:253], v[134:135], 2, s[30:31]
	global_load_dword v244, v[252:253], off
	global_load_dword v245, v[252:253], off offset:64
	global_load_dword v246, v[252:253], off offset:128
	global_load_dword v247, v[252:253], off offset:192
	global_load_dword v248, v[252:253], off offset:512
	global_load_dword v249, v[252:253], off offset:576
	global_load_dword v250, v[252:253], off offset:640
	global_load_dword v251, v[252:253], off offset:704
	s_waitcnt vmcnt(0)
	s_and_saveexec_b64 s[28:29], vcc
	s_cbranch_execz .LBB0_1437
	s_add_u32 s30, s27, s6
	s_addc_u32 s31, s33, s7
	v_lshl_add_u64 v[136:137], v[134:135], 2, s[30:31]
	v_mov_b32_e32 v136, v244
	v_cvt_pk_bf16_f32 v122, v122, v123
	v_cvt_pk_bf16_f32 v123, v124, v125
	v_cvt_pk_bf16_f32 v124, v118, v119
	v_cvt_pk_bf16_f32 v130, v130, v131
	v_cvt_pk_bf16_f32 v131, v132, v133
	v_cvt_pk_bf16_f32 v132, v126, v127
	v_cvt_pk_bf16_f32 v133, v128, v129
	v_cvt_pk_bf16_f32 v125, v120, v121
	v_ashrrev_i32_e32 v137, 31, v136
	v_lshlrev_b64 v[118:119], 12, v[136:137]
	v_lshl_add_u64 v[118:119], s[8:9], 0, v[118:119]
	v_lshl_add_u64 v[118:119], v[4:5], 1, v[118:119]
	global_store_dwordx4 v[118:119], v[130:133], off
	global_store_dwordx4 v[118:119], v[122:125], off offset:256
.LBB0_1437:
	s_or_b64 exec, exec, s[28:29]
	v_or_b32_e32 v118, 16, v134
	v_cmp_lt_i32_e32 vcc, v118, v3
	s_and_saveexec_b64 s[28:29], vcc
	s_cbranch_execz .LBB0_1439
	s_add_u32 s30, s27, s6
	s_addc_u32 s31, s33, s7
	v_lshl_add_u64 v[118:119], v[134:135], 2, s[30:31]
	v_mov_b32_e32 v118, v245
	v_cvt_pk_bf16_f32 v106, v106, v107
	v_cvt_pk_bf16_f32 v107, v108, v109
	v_cvt_pk_bf16_f32 v108, v102, v103
	v_cvt_pk_bf16_f32 v114, v114, v115
	v_cvt_pk_bf16_f32 v115, v116, v117
	v_cvt_pk_bf16_f32 v116, v110, v111
	v_cvt_pk_bf16_f32 v117, v112, v113
	v_cvt_pk_bf16_f32 v109, v104, v105
	v_ashrrev_i32_e32 v119, 31, v118
	v_lshlrev_b64 v[102:103], 12, v[118:119]
	v_lshl_add_u64 v[102:103], s[8:9], 0, v[102:103]
	v_lshl_add_u64 v[102:103], v[4:5], 1, v[102:103]
	global_store_dwordx4 v[102:103], v[114:117], off
	global_store_dwordx4 v[102:103], v[106:109], off offset:256
.LBB0_1439:
	s_or_b64 exec, exec, s[28:29]
	v_or_b32_e32 v102, 32, v134
	v_cmp_lt_i32_e32 vcc, v102, v3
	s_and_saveexec_b64 s[28:29], vcc
	s_cbranch_execz .LBB0_1441
	s_add_u32 s30, s27, s6
	s_addc_u32 s31, s33, s7
	v_lshl_add_u64 v[102:103], v[134:135], 2, s[30:31]
	v_mov_b32_e32 v102, v246
	v_cvt_pk_bf16_f32 v90, v90, v91
	v_cvt_pk_bf16_f32 v91, v92, v93
	v_cvt_pk_bf16_f32 v92, v86, v87
	v_cvt_pk_bf16_f32 v98, v98, v99
	v_cvt_pk_bf16_f32 v99, v100, v101
	v_cvt_pk_bf16_f32 v100, v94, v95
	v_cvt_pk_bf16_f32 v101, v96, v97
	v_cvt_pk_bf16_f32 v93, v88, v89
	v_ashrrev_i32_e32 v103, 31, v102
	v_lshlrev_b64 v[86:87], 12, v[102:103]
	v_lshl_add_u64 v[86:87], s[8:9], 0, v[86:87]
	v_lshl_add_u64 v[86:87], v[4:5], 1, v[86:87]
	global_store_dwordx4 v[86:87], v[98:101], off
	global_store_dwordx4 v[86:87], v[90:93], off offset:256
; __device__ __forceinline__ unsigned cvt_pk_bf16(float lo, float hi) { const f32x2 v = {lo, hi}; return __builtin_bit_cast(unsigned, __builtin_convertvector(v, bf16x2_t)); }
;     __device__ __forceinline__ void operator()(Acc& acc, const GUnit& u, int wr, int wc, int fr, int fq, LAS unsigned char*, int, int) const {
;     ...
;             for (int m = 0; m < 4; ++m) { const int idx = j * 256 + ai * HALF + wr * 64 + m * 16 + fr;
;                 if (idx < n) { const int dest = slot[(size_t)e * CAP + idx]; bf16_t* rowp = Y + (size_t)dest * 2048 + col0;
; #pragma unroll
;                     for (int bj = 0; bj < 2; ++bj) { const f32x4 v0 = acc[ai][bj][m][0], v1 = acc[ai][bj][m][1];
;                         u32x4 w; w.x = cvt_pk_bf16(v0[0], v0[1]); w.y = cvt_pk_bf16(v0[2], v0[3]); w.z = cvt_pk_bf16(v1[0], v1[1]); w.w = cvt_pk_bf16(v1[2], v1[3]);
;                         *(u32x4*)(rowp + bj * HALF) = w; } } }
.LBB0_1441:
	s_or_b64 exec, exec, s[28:29]
	v_or_b32_e32 v86, 48, v134
	v_cmp_lt_i32_e32 vcc, v86, v3
	s_and_saveexec_b64 s[28:29], vcc
	s_cbranch_execz .LBB0_1443
	s_add_u32 s30, s27, s6
	s_addc_u32 s31, s33, s7
	v_lshl_add_u64 v[86:87], v[134:135], 2, s[30:31]
	v_mov_b32_e32 v86, v247
	v_cvt_pk_bf16_f32 v74, v74, v75
	v_cvt_pk_bf16_f32 v75, v76, v77
	v_cvt_pk_bf16_f32 v76, v70, v71
	v_cvt_pk_bf16_f32 v82, v82, v83
	v_cvt_pk_bf16_f32 v83, v84, v85
	v_cvt_pk_bf16_f32 v84, v78, v79
	v_cvt_pk_bf16_f32 v85, v80, v81
	v_cvt_pk_bf16_f32 v77, v72, v73
	v_ashrrev_i32_e32 v87, 31, v86
	v_lshlrev_b64 v[70:71], 12, v[86:87]
	v_lshl_add_u64 v[70:71], s[8:9], 0, v[70:71]
	v_lshl_add_u64 v[70:71], v[4:5], 1, v[70:71]
	global_store_dwordx4 v[70:71], v[82:85], off
	global_store_dwordx4 v[70:71], v[74:77], off offset:256
.LBB0_1443:
	s_or_b64 exec, exec, s[28:29]
	v_add_u32_e32 v70, 0x80, v134
	v_cmp_lt_i32_e32 vcc, v70, v3
	s_and_saveexec_b64 s[28:29], vcc
	s_cbranch_execz .LBB0_1445
	s_add_u32 s30, s27, s6
	s_addc_u32 s31, s33, s7
	v_lshl_add_u64 v[70:71], v[134:135], 2, s[30:31]
	v_mov_b32_e32 v70, v248
	v_cvt_pk_bf16_f32 v58, v58, v59
	v_cvt_pk_bf16_f32 v59, v60, v61
	v_cvt_pk_bf16_f32 v60, v54, v55
	v_cvt_pk_bf16_f32 v66, v66, v67
	v_cvt_pk_bf16_f32 v67, v68, v69
	v_cvt_pk_bf16_f32 v68, v62, v63
	v_cvt_pk_bf16_f32 v69, v64, v65
	v_cvt_pk_bf16_f32 v61, v56, v57
	v_ashrrev_i32_e32 v71, 31, v70
	v_lshlrev_b64 v[54:55], 12, v[70:71]
	v_lshl_add_u64 v[54:55], s[8:9], 0, v[54:55]
	v_lshl_add_u64 v[54:55], v[4:5], 1, v[54:55]
	global_store_dwordx4 v[54:55], v[66:69], off
	global_store_dwordx4 v[54:55], v[58:61], off offset:256
.LBB0_1445:
	s_or_b64 exec, exec, s[28:29]
	v_add_u32_e32 v54, 0x90, v134
	v_cmp_lt_i32_e32 vcc, v54, v3
	s_and_saveexec_b64 s[28:29], vcc
	s_cbranch_execz .LBB0_1447
	s_add_u32 s30, s27, s6
	s_addc_u32 s31, s33, s7
	v_lshl_add_u64 v[54:55], v[134:135], 2, s[30:31]
	v_mov_b32_e32 v54, v249
	v_cvt_pk_bf16_f32 v42, v42, v43
	v_cvt_pk_bf16_f32 v43, v44, v45
	v_cvt_pk_bf16_f32 v44, v38, v39
	v_cvt_pk_bf16_f32 v50, v50, v51
	v_cvt_pk_bf16_f32 v51, v52, v53
	v_cvt_pk_bf16_f32 v52, v46, v47
	v_cvt_pk_bf16_f32 v53, v48, v49
	v_cvt_pk_bf16_f32 v45, v40, v41
	v_ashrrev_i32_e32 v55, 31, v54
	v_lshlrev_b64 v[38:39], 12, v[54:55]
	v_lshl_add_u64 v[38:39], s[8:9], 0, v[38:39]
	v_lshl_add_u64 v[38:39], v[4:5], 1, v[38:39]
	global_store_dwordx4 v[38:39], v[50:53], off
	global_store_dwordx4 v[38:39], v[42:45], off offset:256
.LBB0_1447:
	s_or_b64 exec, exec, s[28:29]
	v_add_u32_e32 v38, 0xa0, v134
	v_cmp_lt_i32_e32 vcc, v38, v3
	s_and_saveexec_b64 s[28:29], vcc
	s_cbranch_execz .LBB0_1449
	s_add_u32 s30, s27, s6
	s_addc_u32 s31, s33, s7
	v_lshl_add_u64 v[38:39], v[134:135], 2, s[30:31]
	v_mov_b32_e32 v38, v250
	v_cvt_pk_bf16_f32 v26, v26, v27
	v_cvt_pk_bf16_f32 v27, v28, v29
	v_cvt_pk_bf16_f32 v28, v22, v23
	v_cvt_pk_bf16_f32 v34, v34, v35
	v_cvt_pk_bf16_f32 v35, v36, v37
	v_cvt_pk_bf16_f32 v36, v30, v31
	v_cvt_pk_bf16_f32 v37, v32, v33
	v_cvt_pk_bf16_f32 v29, v24, v25
	v_ashrrev_i32_e32 v39, 31, v38
	v_lshlrev_b64 v[22:23], 12, v[38:39]
	v_lshl_add_u64 v[22:23], s[8:9], 0, v[22:23]
	v_lshl_add_u64 v[22:23], v[4:5], 1, v[22:23]
	global_store_dwordx4 v[22:23], v[34:37], off
	global_store_dwordx4 v[22:23], v[26:29], off offset:256
.LBB0_1449:
	s_or_b64 exec, exec, s[28:29]
	v_add_u32_e32 v22, 0xb0, v134
	v_cmp_lt_i32_e32 vcc, v22, v3
	s_and_saveexec_b64 s[28:29], vcc
	s_cbranch_execz .LBB0_1451
	s_add_u32 s6, s27, s6
	s_addc_u32 s7, s33, s7
	v_lshl_add_u64 v[22:23], v[134:135], 2, s[6:7]
	v_mov_b32_e32 v22, v251
	v_cvt_pk_bf16_f32 v10, v10, v11
	v_cvt_pk_bf16_f32 v11, v12, v13
	v_cvt_pk_bf16_f32 v12, v6, v7
	v_cvt_pk_bf16_f32 v18, v18, v19
	v_cvt_pk_bf16_f32 v19, v20, v21
	v_cvt_pk_bf16_f32 v20, v14, v15
	v_cvt_pk_bf16_f32 v21, v16, v17
	v_cvt_pk_bf16_f32 v13, v8, v9
	v_ashrrev_i32_e32 v23, 31, v22
	v_lshlrev_b64 v[6:7], 12, v[22:23]
	v_lshl_add_u64 v[6:7], s[8:9], 0, v[6:7]
	v_lshl_add_u64 v[4:5], v[4:5], 1, v[6:7]
	global_store_dwordx4 v[4:5], v[18:21], off
	global_store_dwordx4 v[4:5], v[10:13], off offset:256

; __global__ __launch_bounds__(NTHR, 2) void k_mega(Params p) {
	.amdhsa_kernel _Z6k_mega6Params
		.amdhsa_group_segment_fixed_size 0
		.amdhsa_private_segment_fixed_size 0
		.amdhsa_kernarg_size 480
		.amdhsa_user_sgpr_count 2
		.amdhsa_user_sgpr_dispatch_ptr 0
		.amdhsa_user_sgpr_queue_ptr 0
		.amdhsa_user_sgpr_kernarg_segment_ptr 1
		.amdhsa_user_sgpr_dispatch_id 0
		.amdhsa_user_sgpr_kernarg_preload_length 0
		.amdhsa_user_sgpr_kernarg_preload_offset 0
		.amdhsa_user_sgpr_private_segment_size 0
		.amdhsa_uses_dynamic_stack 0
		.amdhsa_enable_private_segment 0
		.amdhsa_system_sgpr_workgroup_id_x 1
		.amdhsa_system_sgpr_workgroup_id_y 0
		.amdhsa_system_sgpr_workgroup_id_z 0
		.amdhsa_system_sgpr_workgroup_info 0
		.amdhsa_system_vgpr_workitem_id 0
		.amdhsa_next_free_vgpr 256
		.amdhsa_next_free_sgpr 102
		.amdhsa_accum_offset 256
		.amdhsa_reserve_vcc 1
		.amdhsa_float_round_mode_32 0
		.amdhsa_float_round_mode_16_64 0
		.amdhsa_float_denorm_mode_32 3
		.amdhsa_float_denorm_mode_16_64 3
		.amdhsa_dx10_clamp 1
		.amdhsa_ieee_mode 1
		.amdhsa_fp16_overflow 0
		.amdhsa_tg_split 0
		.amdhsa_exception_fp_ieee_invalid_op 0
		.amdhsa_exception_fp_denorm_src 0
		.amdhsa_exception_fp_ieee_div_zero 0
		.amdhsa_exception_fp_ieee_overflow 0
		.amdhsa_exception_fp_ieee_underflow 0
		.amdhsa_exception_fp_ieee_inexact 0
		.amdhsa_exception_int_div_zero 0
	.end_amdhsa_kernel

; __global__ __launch_bounds__(NTHR, 2) void k_mega(Params p) {
amdhsa.kernels:
  - .agpr_count:     0
    .args:
      - .offset:         0
        .size:           224
        .value_kind:     by_value
      - .offset:         224
        .size:           4
        .value_kind:     hidden_block_count_x
      - .offset:         228
        .size:           4
        .value_kind:     hidden_block_count_y
      - .offset:         232
        .size:           4
        .value_kind:     hidden_block_count_z
      - .offset:         236
        .size:           2
        .value_kind:     hidden_group_size_x
      - .offset:         238
        .size:           2
        .value_kind:     hidden_group_size_y
      - .offset:         240
        .size:           2
        .value_kind:     hidden_group_size_z
      - .offset:         242
        .size:           2
        .value_kind:     hidden_remainder_x
      - .offset:         244
        .size:           2
        .value_kind:     hidden_remainder_y
      - .offset:         246
        .size:           2
        .value_kind:     hidden_remainder_z
      - .offset:         264
        .size:           8
        .value_kind:     hidden_global_offset_x
      - .offset:         272
        .size:           8
        .value_kind:     hidden_global_offset_y
      - .offset:         280
        .size:           8
        .value_kind:     hidden_global_offset_z
      - .offset:         288
        .size:           2
        .value_kind:     hidden_grid_dims
      - .offset:         344
        .size:           4
        .value_kind:     hidden_dynamic_lds_size
    .group_segment_fixed_size: 0
    .kernarg_segment_align: 8
    .kernarg_segment_size: 480
    .language:       OpenCL C
    .language_version:
      - 2
      - 0
    .max_flat_workgroup_size: 512
    .name:           _Z6k_mega6Params
    .private_segment_fixed_size: 0
    .sgpr_count:     108
    .sgpr_spill_count: 89
    .symbol:         _Z6k_mega6Params.kd
    .uniform_work_group_size: 1
    .uses_dynamic_stack: false
    .vgpr_count:     256
    .vgpr_spill_count: 0
    .wavefront_size: 64
